# branch GEMM final epilogue: 16 gate loads hoisted ahead of the compute (renamed into free VGPRs, counted vmcnt); stick-breaking lane-group select via v_cndmask
# baseline (speedup 1.0000x reference)
.LBB0_643:
	v_med3_f32 v66, v86, s87, v123
	v_med3_f32 v69, v81, s87, v123
	v_exp_f32_e32 v86, v66
	v_med3_f32 v66, v87, s87, v123
	v_exp_f32_e32 v89, v69
	v_med3_f32 v69, v82, s87, v123
	v_exp_f32_e32 v87, v66
	v_med3_f32 v66, v80, s87, v123
	v_exp_f32_e32 v80, v69
	v_med3_f32 v69, v83, s87, v123
	v_exp_f32_e32 v81, v69
	v_exp_f32_e32 v88, v66
	v_med3_f32 v64, v84, s87, v123
	v_exp_f32_e32 v84, v64
	v_med3_f32 v64, v85, s87, v123
	v_add_f32_e32 v70, 1.0, v80
	v_add_f32_e32 v71, 1.0, v81
	v_exp_f32_e32 v85, v64
	v_add_f32_e32 v69, 1.0, v89
	v_rcp_f32_e32 v70, v70
	v_rcp_f32_e32 v83, v71
	v_add_f32_e32 v68, 1.0, v88
	v_rcp_f32_e32 v69, v69
	v_add_f32_e32 v67, 1.0, v87
	v_rcp_f32_e32 v68, v68
	v_add_f32_e32 v66, 1.0, v86
	v_rcp_f32_e32 v67, v67
	v_add_f32_e32 v65, 1.0, v85
	v_rcp_f32_e32 v66, v66
	v_mul_f32_e32 v82, v70, v83
	v_add_f32_e32 v64, 1.0, v84
	v_rcp_f32_e32 v65, v65
	v_mul_f32_e32 v91, v69, v82
	v_rcp_f32_e32 v64, v64
	v_mul_f32_e32 v90, v68, v91
	v_mul_f32_e32 v93, v67, v90
	v_mul_f32_e32 v92, v66, v93
	v_mul_f32_e32 v95, v65, v92
	v_mul_f32_e32 v94, v64, v95
	ds_bpermute_b32 v70, v132, v94
	ds_bpermute_b32 v71, v133, v94
	ds_bpermute_b32 v65, v134, v94
	ds_bpermute_b32 v64, v135, v94
	s_waitcnt lgkmcnt(0)
	v_mul_f32_e32 v157, v65, v64
	v_mul_f32_e32 v246, v157, v71
	v_cndmask_b32_e64 v158, 1.0, v64, s[14:15]
	v_cndmask_b32_e64 v158, v246, v158, s[18:19]
	v_cndmask_b32_e64 v158, v157, v158, s[16:17]
	v_med3_f32 v64, v76, s87, v123
	v_exp_f32_e32 v66, v64
	v_med3_f32 v64, v77, s87, v123
	v_exp_f32_e32 v67, v64
	v_med3_f32 v72, v72, s87, v123
	v_add_f32_e32 v64, 1.0, v66
	v_rcp_f32_e32 v68, v64
	v_med3_f32 v64, v78, s87, v123
	v_exp_f32_e32 v64, v64
	v_exp_f32_e32 v76, v72
	v_add_f32_e32 v65, 1.0, v67
	v_rcp_f32_e32 v69, v65
	v_add_f32_e32 v72, 1.0, v64
	v_rcp_f32_e32 v96, v72
	v_med3_f32 v72, v73, s87, v123
	v_exp_f32_e32 v77, v72
	v_med3_f32 v72, v74, s87, v123
	v_exp_f32_e32 v72, v72
	v_med3_f32 v73, v75, s87, v123
	v_exp_f32_e32 v73, v73
	v_med3_f32 v65, v79, s87, v123
	v_exp_f32_e32 v65, v65
	v_add_f32_e32 v75, 1.0, v72
	v_rcp_f32_e32 v97, v75
	v_add_f32_e32 v75, 1.0, v73
	v_add_f32_e32 v74, 1.0, v77
	v_rcp_f32_e32 v75, v75
	v_add_f32_e32 v79, 1.0, v76
	v_rcp_f32_e32 v154, v74
	v_add_f32_e32 v78, 1.0, v65
	v_rcp_f32_e32 v155, v79
	v_rcp_f32_e32 v156, v78
	v_mul_f32_e32 v74, v97, v75
	v_mul_f32_e32 v79, v154, v74
	v_mul_f32_e32 v78, v155, v79
	v_mul_f32_e32 v97, v156, v78
	v_mul_f32_e32 v96, v96, v97
	v_mul_f32_e32 v69, v69, v96
	v_mul_f32_e32 v68, v68, v69
	ds_bpermute_b32 v154, v132, v68
	ds_bpermute_b32 v155, v133, v68
	ds_bpermute_b32 v156, v134, v68
	ds_bpermute_b32 v160, v135, v68
	s_waitcnt lgkmcnt(0)
	v_mul_f32_e32 v156, v156, v160
	v_mul_f32_e32 v246, v156, v155
	v_cndmask_b32_e64 v159, 1.0, v160, s[14:15]
	v_cndmask_b32_e64 v159, v246, v159, s[18:19]
	v_cndmask_b32_e64 v159, v156, v159, s[16:17]
	s_and_b64 vcc, exec, s[12:13]
	s_cbranch_vccnz .LBB0_661
	s_waitcnt vmcnt(3)
	ds_write_b128 v98, v[16:19] offset:16384
	s_waitcnt vmcnt(2)
	ds_write_b128 v99, v[20:23] offset:16384
	s_waitcnt vmcnt(1)
	ds_write_b128 v100, v[24:27] offset:32768
	s_waitcnt vmcnt(0)
	ds_write_b128 v124, v[28:31] offset:32768

.LBB0_667:
	v_med3_f32 v73, v73, s87, v123
	v_exp_f32_e32 v73, v73
	v_med3_f32 v78, v78, s87, v123
	v_exp_f32_e32 v78, v78
	v_med3_f32 v79, v79, s87, v123
	v_med3_f32 v72, v72, s87, v123
	v_med3_f32 v77, v77, s87, v123
	v_exp_f32_e32 v79, v79
	v_exp_f32_e32 v72, v72
	v_med3_f32 v74, v74, s87, v123
	v_med3_f32 v76, v76, s87, v123
	v_exp_f32_e32 v77, v77
	v_add_f32_e32 v81, 1.0, v73
	v_exp_f32_e32 v74, v74
	v_med3_f32 v75, v75, s87, v123
	v_exp_f32_e32 v76, v76
	v_rcp_f32_e32 v87, v81
	v_exp_f32_e32 v75, v75
	v_add_f32_e32 v81, 1.0, v78
	v_rcp_f32_e32 v85, v81
	v_add_f32_e32 v81, 1.0, v79
	v_add_f32_e32 v80, 1.0, v72
	v_add_f32_e32 v83, 1.0, v77
	v_rcp_f32_e32 v81, v81
	v_rcp_f32_e32 v86, v80
	v_add_f32_e32 v80, 1.0, v74
	v_add_f32_e32 v82, 1.0, v76
	v_rcp_f32_e32 v83, v83
	v_rcp_f32_e32 v84, v80
	v_add_f32_e32 v80, 1.0, v75
	v_rcp_f32_e32 v82, v82
	v_rcp_f32_e32 v88, v80
	v_mul_f32_e32 v80, v85, v81
	v_mul_f32_e32 v83, v83, v80
	v_mul_f32_e32 v82, v82, v83
	v_mul_f32_e32 v85, v88, v82
	v_mul_f32_e32 v84, v84, v85
	v_mul_f32_e32 v87, v87, v84
	v_mul_f32_e32 v86, v86, v87
	ds_bpermute_b32 v96, v132, v86
	ds_bpermute_b32 v97, v133, v86
	ds_bpermute_b32 v89, v134, v86
	ds_bpermute_b32 v88, v135, v86
	s_waitcnt lgkmcnt(0)
	v_mul_f32_e32 v159, v89, v88
	v_mul_f32_e32 v246, v159, v97
	v_cndmask_b32_e64 v158, 1.0, v88, s[14:15]
	v_cndmask_b32_e64 v158, v246, v158, s[18:19]
	v_cndmask_b32_e64 v158, v159, v158, s[16:17]
	v_med3_f32 v69, v69, s87, v123
	v_exp_f32_e32 v69, v69
	v_med3_f32 v66, v66, s87, v123
	v_exp_f32_e32 v66, v66
	v_med3_f32 v67, v67, s87, v123
	v_med3_f32 v68, v68, s87, v123
	v_med3_f32 v65, v65, s87, v123
	v_exp_f32_e32 v67, v67
	v_exp_f32_e32 v68, v68
	v_med3_f32 v70, v70, s87, v123
	v_med3_f32 v64, v64, s87, v123
	v_exp_f32_e32 v65, v65
	v_add_f32_e32 v89, 1.0, v69
	v_exp_f32_e32 v70, v70
	v_med3_f32 v71, v71, s87, v123
	v_exp_f32_e32 v64, v64
	v_rcp_f32_e32 v95, v89
	v_exp_f32_e32 v71, v71
	v_add_f32_e32 v89, 1.0, v66
	v_rcp_f32_e32 v93, v89
	v_add_f32_e32 v89, 1.0, v67
	v_add_f32_e32 v88, 1.0, v68
	v_add_f32_e32 v91, 1.0, v65
	v_rcp_f32_e32 v89, v89
	v_rcp_f32_e32 v94, v88
	v_add_f32_e32 v88, 1.0, v70
	v_add_f32_e32 v90, 1.0, v64
	v_rcp_f32_e32 v91, v91
	v_rcp_f32_e32 v92, v88
	v_add_f32_e32 v88, 1.0, v71
	v_rcp_f32_e32 v90, v90
	v_rcp_f32_e32 v160, v88
	v_mul_f32_e32 v88, v93, v89
	v_mul_f32_e32 v91, v91, v88
	v_mul_f32_e32 v90, v90, v91
	v_mul_f32_e32 v93, v160, v90
	v_mul_f32_e32 v92, v92, v93
	v_mul_f32_e32 v95, v95, v92
	v_mul_f32_e32 v94, v94, v95
	ds_bpermute_b32 v160, v132, v94
	ds_bpermute_b32 v161, v133, v94
	ds_bpermute_b32 v163, v134, v94
	ds_bpermute_b32 v162, v135, v94
	s_waitcnt lgkmcnt(0)
	v_mul_f32_e32 v163, v163, v162
	v_mul_f32_e32 v246, v163, v161
	v_cndmask_b32_e64 v164, 1.0, v162, s[14:15]
	v_cndmask_b32_e64 v164, v246, v164, s[18:19]
	v_cndmask_b32_e64 v164, v163, v164, s[16:17]
	s_and_b64 vcc, exec, s[12:13]
	s_cbranch_vccnz .LBB0_685
	s_waitcnt vmcnt(3)
	ds_write_b128 v98, v[16:19]
	s_waitcnt vmcnt(2)
	ds_write_b128 v99, v[20:23]
	s_waitcnt vmcnt(1)
	ds_write_b128 v100, v[24:27] offset:49152
	s_waitcnt vmcnt(0)
	ds_write_b128 v124, v[28:31] offset:49152

.LBB0_770:
	v_med3_f32 v73, v73, s87, v123
	v_exp_f32_e32 v73, v73
	v_med3_f32 v78, v78, s87, v123
	v_exp_f32_e32 v78, v78
	v_med3_f32 v79, v79, s87, v123
	v_med3_f32 v72, v72, s87, v123
	v_med3_f32 v77, v77, s87, v123
	v_exp_f32_e32 v79, v79
	v_exp_f32_e32 v72, v72
	v_med3_f32 v74, v74, s87, v123
	v_med3_f32 v76, v76, s87, v123
	v_exp_f32_e32 v77, v77
	v_add_f32_e32 v81, 1.0, v73
	v_exp_f32_e32 v74, v74
	v_med3_f32 v75, v75, s87, v123
	v_exp_f32_e32 v76, v76
	v_rcp_f32_e32 v87, v81
	v_exp_f32_e32 v75, v75
	v_add_f32_e32 v81, 1.0, v78
	v_rcp_f32_e32 v85, v81
	v_add_f32_e32 v81, 1.0, v79
	v_add_f32_e32 v80, 1.0, v72
	v_add_f32_e32 v83, 1.0, v77
	v_rcp_f32_e32 v81, v81
	v_rcp_f32_e32 v86, v80
	v_add_f32_e32 v80, 1.0, v74
	v_add_f32_e32 v82, 1.0, v76
	v_rcp_f32_e32 v83, v83
	v_rcp_f32_e32 v84, v80
	v_add_f32_e32 v80, 1.0, v75
	v_rcp_f32_e32 v82, v82
	v_rcp_f32_e32 v88, v80
	v_mul_f32_e32 v80, v85, v81
	v_mul_f32_e32 v83, v83, v80
	v_mul_f32_e32 v82, v82, v83
	v_mul_f32_e32 v85, v88, v82
	v_mul_f32_e32 v84, v84, v85
	v_mul_f32_e32 v87, v87, v84
	v_mul_f32_e32 v86, v86, v87
	ds_bpermute_b32 v96, v132, v86
	ds_bpermute_b32 v97, v133, v86
	ds_bpermute_b32 v89, v134, v86
	ds_bpermute_b32 v88, v135, v86
	s_waitcnt lgkmcnt(0)
	v_mul_f32_e32 v159, v89, v88
	v_mul_f32_e32 v246, v159, v97
	v_cndmask_b32_e64 v158, 1.0, v88, s[14:15]
	v_cndmask_b32_e64 v158, v246, v158, s[18:19]
	v_cndmask_b32_e64 v158, v159, v158, s[16:17]
	v_med3_f32 v69, v69, s87, v123
	v_exp_f32_e32 v69, v69
	v_med3_f32 v68, v68, s87, v123
	v_exp_f32_e32 v68, v68
	v_med3_f32 v65, v65, s87, v123
	v_add_f32_e32 v89, 1.0, v69
	v_rcp_f32_e32 v161, v89
	v_exp_f32_e32 v89, v65
	v_med3_f32 v65, v66, s87, v123
	v_exp_f32_e32 v90, v65
	v_med3_f32 v65, v67, s87, v123
	v_exp_f32_e32 v91, v65
	v_add_f32_e32 v88, 1.0, v68
	v_med3_f32 v64, v64, s87, v123
	v_rcp_f32_e32 v160, v88
	v_med3_f32 v71, v71, s87, v123
	v_exp_f32_e32 v88, v64
	v_med3_f32 v70, v70, s87, v123
	v_exp_f32_e32 v71, v71
	v_exp_f32_e32 v70, v70
	v_add_f32_e32 v66, 1.0, v90
	v_add_f32_e32 v67, 1.0, v91
	v_add_f32_e32 v65, 1.0, v89
	v_rcp_f32_e32 v66, v66
	v_rcp_f32_e32 v93, v67
	v_add_f32_e32 v94, 1.0, v88
	v_rcp_f32_e32 v65, v65
	v_add_f32_e32 v92, 1.0, v71
	v_rcp_f32_e32 v94, v94
	v_add_f32_e32 v64, 1.0, v70
	v_rcp_f32_e32 v95, v92
	v_rcp_f32_e32 v64, v64
	v_mul_f32_e32 v92, v66, v93
	v_mul_f32_e32 v67, v65, v92
	v_mul_f32_e32 v66, v94, v67
	v_mul_f32_e32 v95, v95, v66
	v_mul_f32_e32 v94, v64, v95
	v_mul_f32_e32 v65, v161, v94
	v_mul_f32_e32 v64, v160, v65
	ds_bpermute_b32 v160, v132, v64
	ds_bpermute_b32 v161, v133, v64
	ds_bpermute_b32 v163, v134, v64
	ds_bpermute_b32 v162, v135, v64
	s_waitcnt lgkmcnt(0)
	v_mul_f32_e32 v163, v163, v162
	v_mul_f32_e32 v246, v163, v161
	v_cndmask_b32_e64 v164, 1.0, v162, s[14:15]
	v_cndmask_b32_e64 v164, v246, v164, s[18:19]
	v_cndmask_b32_e64 v164, v163, v164, s[16:17]
	s_and_b64 vcc, exec, s[12:13]
	s_cbranch_vccnz .LBB0_788
	s_waitcnt vmcnt(3)
	ds_write_b128 v98, v[16:19]
	s_waitcnt vmcnt(2)
	ds_write_b128 v99, v[20:23]
	s_waitcnt vmcnt(1)
	ds_write_b128 v100, v[24:27] offset:49152
	s_waitcnt vmcnt(0)
	ds_write_b128 v124, v[28:31] offset:49152

.LBB0_894:
	v_mov_b64_e32 v[146:147], s[22:23]
	v_mad_i64_i32 v[244:245], s[36:37], v128, s46, v[146:147]
	v_lshl_or_b32 v138, s52, 8, v153
	v_ashrrev_i32_e32 v139, 31, v138
	v_lshlrev_b64 v[242:243], 1, v[138:139]
	v_lshl_add_u64 v[240:241], v[244:245], 0, v[242:243]
	global_load_dwordx4 v[140:143], v[240:241], off
	global_load_dwordx4 v[160:163], v[240:241], off offset:256
	v_or_b32_e32 v244, 16, v128
	v_mad_i64_i32 v[138:139], s[36:37], v244, s46, v[146:147]
	v_lshl_add_u64 v[240:241], v[138:139], 0, v[242:243]
	global_load_dwordx4 v[164:167], v[240:241], off
	global_load_dwordx4 v[168:171], v[240:241], off offset:256
	v_or_b32_e32 v138, 32, v128
	v_mad_i64_i32 v[238:239], s[36:37], v138, s46, v[146:147]
	v_lshl_add_u64 v[240:241], v[238:239], 0, v[242:243]
	global_load_dwordx4 v[172:175], v[240:241], off
	global_load_dwordx4 v[176:179], v[240:241], off offset:256
	v_or_b32_e32 v238, 48, v128
	v_mad_i64_i32 v[236:237], s[36:37], v238, s46, v[146:147]
	v_lshl_add_u64 v[240:241], v[236:237], 0, v[242:243]
	global_load_dwordx4 v[180:183], v[240:241], off
	global_load_dwordx4 v[184:187], v[240:241], off offset:256
	v_add_u32_e32 v236, 0x80, v128
	v_mad_i64_i32 v[234:235], s[36:37], v236, s46, v[146:147]
	v_lshl_add_u64 v[240:241], v[234:235], 0, v[242:243]
	global_load_dwordx4 v[188:191], v[240:241], off
	global_load_dwordx4 v[192:195], v[240:241], off offset:256
	v_add_u32_e32 v234, 0x90, v128
	v_mad_i64_i32 v[232:233], s[36:37], v234, s46, v[146:147]
	v_lshl_add_u64 v[240:241], v[232:233], 0, v[242:243]
	global_load_dwordx4 v[196:199], v[240:241], off
	global_load_dwordx4 v[200:203], v[240:241], off offset:256
	v_ashrrev_i32_e32 v129, 31, v128
	v_lshlrev_b64 v[232:233], 12, v[128:129]
	v_lshl_add_u64 v[240:241], s[14:15], 0, v[232:233]
	v_lshl_add_u64 v[230:231], v[240:241], 0, v[242:243]
	s_waitcnt vmcnt(11)
	v_lshlrev_b32_e32 v228, 16, v140
	v_and_b32_e32 v229, 0xffff0000, v140
	v_lshlrev_b32_e32 v240, 16, v141
	v_and_b32_e32 v241, 0xffff0000, v141
	v_lshlrev_b32_e32 v232, 16, v142
	v_and_b32_e32 v233, 0xffff0000, v142
	v_lshlrev_b32_e32 v226, 16, v143
	v_and_b32_e32 v227, 0xffff0000, v143
	v_pk_mul_f32 v[224:225], v[108:109], v[228:229]
	v_pk_mul_f32 v[222:223], v[110:111], v[240:241]
	v_pk_mul_f32 v[220:221], v[104:105], v[232:233]
	v_pk_mul_f32 v[228:229], v[106:107], v[226:227]
	v_cvt_pk_bf16_f32 v140, v224, v225
	v_cvt_pk_bf16_f32 v141, v222, v223
	v_cvt_pk_bf16_f32 v142, v220, v221
	v_cvt_pk_bf16_f32 v143, v228, v229
	global_store_dwordx4 v[230:231], v[140:143], off
	v_add_u32_e32 v240, 0xa0, v128
	v_mad_i64_i32 v[232:233], s[36:37], v240, s46, v[146:147]
	v_lshl_add_u64 v[228:229], v[232:233], 0, v[242:243]
	global_load_dwordx4 v[140:143], v[228:229], off
	v_ashrrev_i32_e32 v245, 31, v244
	v_lshlrev_b64 v[232:233], 12, v[244:245]
	v_lshl_add_u64 v[226:227], s[14:15], 0, v[232:233]
	v_lshl_add_u64 v[224:225], v[226:227], 0, v[242:243]
	s_waitcnt vmcnt(12)
	v_lshlrev_b32_e32 v244, 16, v160
	v_and_b32_e32 v245, 0xffff0000, v160
	v_lshlrev_b32_e32 v232, 16, v161
	v_and_b32_e32 v233, 0xffff0000, v161
	v_lshlrev_b32_e32 v226, 16, v162
	v_and_b32_e32 v227, 0xffff0000, v162
	v_lshlrev_b32_e32 v222, 16, v163
	v_and_b32_e32 v223, 0xffff0000, v163
	v_pk_mul_f32 v[220:221], v[76:77], v[244:245]
	v_pk_mul_f32 v[218:219], v[78:79], v[232:233]
	v_pk_mul_f32 v[216:217], v[72:73], v[226:227]
	v_pk_mul_f32 v[244:245], v[74:75], v[222:223]
	v_cvt_pk_bf16_f32 v160, v220, v221
	v_cvt_pk_bf16_f32 v161, v218, v219
	v_cvt_pk_bf16_f32 v162, v216, v217
	v_cvt_pk_bf16_f32 v163, v244, v245
	global_store_dwordx4 v[230:231], v[160:163], off offset:256
	global_load_dwordx4 v[204:207], v[228:229], off offset:256
	s_waitcnt vmcnt(13)
	v_lshlrev_b32_e32 v232, 16, v164
	v_and_b32_e32 v233, 0xffff0000, v164
	v_lshlrev_b32_e32 v226, 16, v165
	v_and_b32_e32 v227, 0xffff0000, v165
	v_lshlrev_b32_e32 v244, 16, v166
	v_and_b32_e32 v245, 0xffff0000, v166
	v_lshlrev_b32_e32 v230, 16, v167
	v_and_b32_e32 v231, 0xffff0000, v167
	v_pk_mul_f32 v[228:229], v[100:101], v[232:233]
	v_pk_mul_f32 v[222:223], v[102:103], v[226:227]
	v_pk_mul_f32 v[220:221], v[96:97], v[244:245]
	v_pk_mul_f32 v[232:233], v[98:99], v[230:231]
	v_cvt_pk_bf16_f32 v160, v228, v229
	v_cvt_pk_bf16_f32 v161, v222, v223
	v_cvt_pk_bf16_f32 v162, v220, v221
	v_cvt_pk_bf16_f32 v163, v232, v233
	global_store_dwordx4 v[224:225], v[160:163], off
	v_add_u32_e32 v226, 0xb0, v128
	v_mad_i64_i32 v[232:233], s[36:37], v226, s46, v[146:147]
	v_lshl_add_u64 v[244:245], v[232:233], 0, v[242:243]
	global_load_dwordx4 v[162:165], v[244:245], off
	v_ashrrev_i32_e32 v139, 31, v138
	s_waitcnt vmcnt(14)
	v_lshlrev_b32_e32 v232, 16, v168
	v_and_b32_e32 v233, 0xffff0000, v168
	v_lshlrev_b32_e32 v166, 16, v169
	v_and_b32_e32 v167, 0xffff0000, v169
	v_lshlrev_b32_e32 v160, 16, v170
	v_and_b32_e32 v161, 0xffff0000, v170
	v_lshlrev_b32_e32 v146, 16, v171
	v_and_b32_e32 v147, 0xffff0000, v171
	v_pk_mul_f32 v[230:231], v[68:69], v[232:233]
	v_pk_mul_f32 v[228:229], v[70:71], v[166:167]
	v_pk_mul_f32 v[222:223], v[64:65], v[160:161]
	v_pk_mul_f32 v[232:233], v[66:67], v[146:147]
	v_cvt_pk_bf16_f32 v168, v230, v231
	v_cvt_pk_bf16_f32 v169, v228, v229
	v_cvt_pk_bf16_f32 v170, v222, v223
	v_cvt_pk_bf16_f32 v171, v232, v233
	global_store_dwordx4 v[224:225], v[168:171], off offset:256
	global_load_dwordx4 v[210:213], v[244:245], off offset:256
	v_lshlrev_b64 v[232:233], 12, v[138:139]
	v_lshl_add_u64 v[224:225], s[14:15], 0, v[232:233]
	v_lshl_add_u64 v[214:215], v[224:225], 0, v[242:243]
	s_waitcnt vmcnt(15)
	v_lshlrev_b32_e32 v208, 16, v172
	v_and_b32_e32 v209, 0xffff0000, v172
	v_lshlrev_b32_e32 v232, 16, v173
	v_and_b32_e32 v233, 0xffff0000, v173
	v_lshlrev_b32_e32 v224, 16, v174
	v_and_b32_e32 v225, 0xffff0000, v174
	v_lshlrev_b32_e32 v166, 16, v175
	v_and_b32_e32 v167, 0xffff0000, v175
	v_pk_mul_f32 v[160:161], v[92:93], v[208:209]
	v_pk_mul_f32 v[146:147], v[94:95], v[232:233]
	v_pk_mul_f32 v[244:245], v[88:89], v[224:225]
	v_pk_mul_f32 v[208:209], v[90:91], v[166:167]
	v_cvt_pk_bf16_f32 v168, v160, v161
	v_cvt_pk_bf16_f32 v169, v146, v147
	v_cvt_pk_bf16_f32 v170, v244, v245
	v_cvt_pk_bf16_f32 v171, v208, v209
	global_store_dwordx4 v[214:215], v[168:171], off
	v_ashrrev_i32_e32 v239, 31, v238
	s_waitcnt vmcnt(15)
	v_lshlrev_b32_e32 v232, 16, v176
	v_and_b32_e32 v233, 0xffff0000, v176
	v_lshlrev_b32_e32 v224, 16, v177
	v_and_b32_e32 v225, 0xffff0000, v177
	v_lshlrev_b32_e32 v208, 16, v178
	v_and_b32_e32 v209, 0xffff0000, v178
	v_lshlrev_b32_e32 v166, 16, v179
	v_and_b32_e32 v167, 0xffff0000, v179
	v_pk_mul_f32 v[160:161], v[60:61], v[232:233]
	v_pk_mul_f32 v[146:147], v[62:63], v[224:225]
	v_pk_mul_f32 v[244:245], v[56:57], v[208:209]
	v_pk_mul_f32 v[232:233], v[58:59], v[166:167]
	v_cvt_pk_bf16_f32 v168, v160, v161
	v_cvt_pk_bf16_f32 v169, v146, v147
	v_cvt_pk_bf16_f32 v170, v244, v245
	v_cvt_pk_bf16_f32 v171, v232, v233
	global_store_dwordx4 v[214:215], v[168:171], off offset:256
	v_lshlrev_b64 v[224:225], 12, v[238:239]
	v_lshl_add_u64 v[232:233], s[14:15], 0, v[224:225]
	v_lshl_add_u64 v[214:215], v[232:233], 0, v[242:243]
	s_waitcnt vmcnt(15)
	v_lshlrev_b32_e32 v238, 16, v180
	v_and_b32_e32 v239, 0xffff0000, v180
	v_lshlrev_b32_e32 v232, 16, v181
	v_and_b32_e32 v233, 0xffff0000, v181
	v_lshlrev_b32_e32 v224, 16, v182
	v_and_b32_e32 v225, 0xffff0000, v182
	v_lshlrev_b32_e32 v208, 16, v183
	v_and_b32_e32 v209, 0xffff0000, v183
	v_pk_mul_f32 v[166:167], v[84:85], v[238:239]
	v_pk_mul_f32 v[160:161], v[86:87], v[232:233]
	v_pk_mul_f32 v[146:147], v[80:81], v[224:225]
	v_pk_mul_f32 v[238:239], v[82:83], v[208:209]
	v_cvt_pk_bf16_f32 v168, v166, v167
	v_cvt_pk_bf16_f32 v169, v160, v161
	v_cvt_pk_bf16_f32 v170, v146, v147
	v_cvt_pk_bf16_f32 v171, v238, v239
	global_store_dwordx4 v[214:215], v[168:171], off
	v_ashrrev_i32_e32 v237, 31, v236
	s_waitcnt vmcnt(15)
	v_lshlrev_b32_e32 v238, 16, v184
	v_and_b32_e32 v239, 0xffff0000, v184
	v_lshlrev_b32_e32 v232, 16, v185
	v_and_b32_e32 v233, 0xffff0000, v185
	v_lshlrev_b32_e32 v224, 16, v186
	v_and_b32_e32 v225, 0xffff0000, v186
	v_lshlrev_b32_e32 v208, 16, v187
	v_and_b32_e32 v209, 0xffff0000, v187
	v_pk_mul_f32 v[166:167], v[52:53], v[238:239]
	v_pk_mul_f32 v[160:161], v[54:55], v[232:233]
	v_pk_mul_f32 v[146:147], v[48:49], v[224:225]
	v_pk_mul_f32 v[238:239], v[50:51], v[208:209]
	v_cvt_pk_bf16_f32 v168, v166, v167
	v_cvt_pk_bf16_f32 v169, v160, v161
	v_cvt_pk_bf16_f32 v170, v146, v147
	v_cvt_pk_bf16_f32 v171, v238, v239
	global_store_dwordx4 v[214:215], v[168:171], off offset:256
	v_lshlrev_b64 v[232:233], 12, v[236:237]
	v_lshl_add_u64 v[224:225], s[14:15], 0, v[232:233]
	v_lshl_add_u64 v[214:215], v[224:225], 0, v[242:243]
	s_waitcnt vmcnt(15)
	v_lshlrev_b32_e32 v208, 16, v188
	v_and_b32_e32 v209, 0xffff0000, v188
	v_lshlrev_b32_e32 v232, 16, v189
	v_and_b32_e32 v233, 0xffff0000, v189
	v_lshlrev_b32_e32 v224, 16, v190
	v_and_b32_e32 v225, 0xffff0000, v190
	v_lshlrev_b32_e32 v166, 16, v191
	v_and_b32_e32 v167, 0xffff0000, v191
	v_pk_mul_f32 v[160:161], v[44:45], v[208:209]
	v_pk_mul_f32 v[146:147], v[46:47], v[232:233]
	v_pk_mul_f32 v[244:245], v[40:41], v[224:225]
	v_pk_mul_f32 v[208:209], v[42:43], v[166:167]
	v_cvt_pk_bf16_f32 v168, v160, v161
	v_cvt_pk_bf16_f32 v169, v146, v147
	v_cvt_pk_bf16_f32 v170, v244, v245
	v_cvt_pk_bf16_f32 v171, v208, v209
	global_store_dwordx4 v[214:215], v[168:171], off
	v_ashrrev_i32_e32 v235, 31, v234
	s_waitcnt vmcnt(15)
	v_lshlrev_b32_e32 v232, 16, v192
	v_and_b32_e32 v233, 0xffff0000, v192
	v_lshlrev_b32_e32 v224, 16, v193
	v_and_b32_e32 v225, 0xffff0000, v193
	v_lshlrev_b32_e32 v208, 16, v194
	v_and_b32_e32 v209, 0xffff0000, v194
	v_lshlrev_b32_e32 v166, 16, v195
	v_and_b32_e32 v167, 0xffff0000, v195
	v_pk_mul_f32 v[160:161], v[12:13], v[232:233]
	v_pk_mul_f32 v[146:147], v[14:15], v[224:225]
	v_pk_mul_f32 v[244:245], v[8:9], v[208:209]
	v_pk_mul_f32 v[232:233], v[10:11], v[166:167]
	v_cvt_pk_bf16_f32 v168, v160, v161
	v_cvt_pk_bf16_f32 v169, v146, v147
	v_cvt_pk_bf16_f32 v170, v244, v245
	v_cvt_pk_bf16_f32 v171, v232, v233
	global_store_dwordx4 v[214:215], v[168:171], off offset:256
	v_lshlrev_b64 v[224:225], 12, v[234:235]
	v_lshl_add_u64 v[208:209], s[14:15], 0, v[224:225]
	v_lshl_add_u64 v[214:215], v[208:209], 0, v[242:243]
	s_waitcnt vmcnt(15)
	v_lshlrev_b32_e32 v166, 16, v196
	v_and_b32_e32 v167, 0xffff0000, v196
	v_lshlrev_b32_e32 v224, 16, v197
	v_and_b32_e32 v225, 0xffff0000, v197
	v_lshlrev_b32_e32 v208, 16, v198
	v_and_b32_e32 v209, 0xffff0000, v198
	v_lshlrev_b32_e32 v160, 16, v199
	v_and_b32_e32 v161, 0xffff0000, v199
	v_pk_mul_f32 v[146:147], v[36:37], v[166:167]
	v_pk_mul_f32 v[244:245], v[38:39], v[224:225]
	v_pk_mul_f32 v[138:139], v[32:33], v[208:209]
	v_pk_mul_f32 v[166:167], v[34:35], v[160:161]
	v_cvt_pk_bf16_f32 v168, v146, v147
	v_cvt_pk_bf16_f32 v169, v244, v245
	v_cvt_pk_bf16_f32 v170, v138, v139
	v_cvt_pk_bf16_f32 v171, v166, v167
	global_store_dwordx4 v[214:215], v[168:171], off
	v_ashrrev_i32_e32 v241, 31, v240
	s_waitcnt vmcnt(15)
	v_lshlrev_b32_e32 v224, 16, v200
	v_and_b32_e32 v225, 0xffff0000, v200
	v_lshlrev_b32_e32 v208, 16, v201
	v_and_b32_e32 v209, 0xffff0000, v201
	v_lshlrev_b32_e32 v166, 16, v202
	v_and_b32_e32 v167, 0xffff0000, v202
	v_lshlrev_b32_e32 v160, 16, v203
	v_and_b32_e32 v161, 0xffff0000, v203
	v_pk_mul_f32 v[146:147], v[4:5], v[224:225]
	v_pk_mul_f32 v[244:245], v[6:7], v[208:209]
	v_pk_mul_f32 v[138:139], v[0:1], v[166:167]
	v_pk_mul_f32 v[224:225], v[2:3], v[160:161]
	v_cvt_pk_bf16_f32 v168, v146, v147
	v_cvt_pk_bf16_f32 v169, v244, v245
	v_cvt_pk_bf16_f32 v170, v138, v139
	v_cvt_pk_bf16_f32 v171, v224, v225
	global_store_dwordx4 v[214:215], v[168:171], off offset:256
	v_lshlrev_b64 v[208:209], 12, v[240:241]
	v_lshl_add_u64 v[224:225], s[14:15], 0, v[208:209]
	v_lshl_add_u64 v[214:215], v[224:225], 0, v[242:243]
	s_waitcnt vmcnt(14)
	v_lshlrev_b32_e32 v240, 16, v140
	v_and_b32_e32 v241, 0xffff0000, v140
	v_lshlrev_b32_e32 v224, 16, v141
	v_and_b32_e32 v225, 0xffff0000, v141
	v_lshlrev_b32_e32 v208, 16, v142
	v_and_b32_e32 v209, 0xffff0000, v142
	v_lshlrev_b32_e32 v166, 16, v143
	v_and_b32_e32 v167, 0xffff0000, v143
	v_pk_mul_f32 v[160:161], v[28:29], v[240:241]
	v_pk_mul_f32 v[146:147], v[30:31], v[224:225]
	v_pk_mul_f32 v[244:245], v[24:25], v[208:209]
	v_pk_mul_f32 v[240:241], v[26:27], v[166:167]
	v_cvt_pk_bf16_f32 v140, v160, v161
	v_cvt_pk_bf16_f32 v141, v146, v147
	v_cvt_pk_bf16_f32 v142, v244, v245
	v_cvt_pk_bf16_f32 v143, v240, v241
	global_store_dwordx4 v[214:215], v[140:143], off
	v_ashrrev_i32_e32 v227, 31, v226
	s_waitcnt vmcnt(13)
	v_lshlrev_b32_e32 v240, 16, v204
	v_and_b32_e32 v241, 0xffff0000, v204
	v_lshlrev_b32_e32 v224, 16, v205
	v_and_b32_e32 v225, 0xffff0000, v205
	v_lshlrev_b32_e32 v208, 16, v206
	v_and_b32_e32 v209, 0xffff0000, v206
	v_lshlrev_b32_e32 v166, 16, v207
	v_and_b32_e32 v167, 0xffff0000, v207
	v_pk_mul_f32 v[160:161], v[112:113], v[240:241]
	v_pk_mul_f32 v[146:147], v[114:115], v[224:225]
	v_pk_mul_f32 v[244:245], v[116:117], v[208:209]
	v_pk_mul_f32 v[240:241], v[118:119], v[166:167]
	v_cvt_pk_bf16_f32 v138, v160, v161
	v_cvt_pk_bf16_f32 v139, v146, v147
	v_cvt_pk_bf16_f32 v140, v244, v245
	v_cvt_pk_bf16_f32 v141, v240, v241
	global_store_dwordx4 v[214:215], v[138:141], off offset:256
	v_lshlrev_b64 v[224:225], 12, v[226:227]
	v_lshl_add_u64 v[240:241], s[14:15], 0, v[224:225]
	v_lshl_add_u64 v[130:131], v[240:241], 0, v[242:243]
	s_waitcnt vmcnt(12)
	v_lshlrev_b32_e32 v214, 16, v162
	v_and_b32_e32 v215, 0xffff0000, v162
	v_lshlrev_b32_e32 v208, 16, v163
	v_and_b32_e32 v209, 0xffff0000, v163
	v_lshlrev_b32_e32 v166, 16, v164
	v_and_b32_e32 v167, 0xffff0000, v164
	v_lshlrev_b32_e32 v160, 16, v165
	v_and_b32_e32 v161, 0xffff0000, v165
	v_pk_mul_f32 v[146:147], v[20:21], v[214:215]
	v_pk_mul_f32 v[244:245], v[22:23], v[208:209]
	v_pk_mul_f32 v[164:165], v[16:17], v[166:167]
	v_pk_mul_f32 v[214:215], v[18:19], v[160:161]
	v_cvt_pk_bf16_f32 v138, v146, v147
	v_cvt_pk_bf16_f32 v139, v244, v245
	v_cvt_pk_bf16_f32 v140, v164, v165
	v_cvt_pk_bf16_f32 v141, v214, v215
	global_store_dwordx4 v[130:131], v[138:141], off
	s_waitcnt vmcnt(11)
	v_lshlrev_b32_e32 v208, 16, v210
	v_and_b32_e32 v209, 0xffff0000, v210
	v_lshlrev_b32_e32 v214, 16, v211
	v_and_b32_e32 v215, 0xffff0000, v211
	v_lshlrev_b32_e32 v146, 16, v212
	v_and_b32_e32 v147, 0xffff0000, v212
	v_lshlrev_b32_e32 v244, 16, v213
	v_and_b32_e32 v245, 0xffff0000, v213
	v_pk_mul_f32 v[138:139], v[120:121], v[208:209]
	v_pk_mul_f32 v[242:243], v[122:123], v[214:215]
	v_pk_mul_f32 v[240:241], v[124:125], v[146:147]
	v_pk_mul_f32 v[238:239], v[126:127], v[244:245]
	v_cvt_pk_bf16_f32 v162, v138, v139
	v_cvt_pk_bf16_f32 v163, v242, v243
	v_cvt_pk_bf16_f32 v164, v240, v241
	v_cvt_pk_bf16_f32 v165, v238, v239
	global_store_dwordx4 v[130:131], v[162:165], off offset:256
	s_cbranch_execnz .LBB0_893

.LBB0_2034:
	v_med3_f32 v66, v86, s55, v123
	v_med3_f32 v69, v81, s55, v123
	v_exp_f32_e32 v86, v66
	v_med3_f32 v66, v87, s55, v123
	v_exp_f32_e32 v89, v69
	v_med3_f32 v69, v82, s55, v123
	v_exp_f32_e32 v87, v66
	v_med3_f32 v66, v80, s55, v123
	v_exp_f32_e32 v80, v69
	v_med3_f32 v69, v83, s55, v123
	v_exp_f32_e32 v81, v69
	v_exp_f32_e32 v88, v66
	v_med3_f32 v64, v84, s55, v123
	v_exp_f32_e32 v84, v64
	v_med3_f32 v64, v85, s55, v123
	v_add_f32_e32 v70, 1.0, v80
	v_add_f32_e32 v71, 1.0, v81
	v_exp_f32_e32 v85, v64
	v_add_f32_e32 v69, 1.0, v89
	v_rcp_f32_e32 v70, v70
	v_rcp_f32_e32 v83, v71
	v_add_f32_e32 v68, 1.0, v88
	v_rcp_f32_e32 v69, v69
	v_add_f32_e32 v67, 1.0, v87
	v_rcp_f32_e32 v68, v68
	v_add_f32_e32 v66, 1.0, v86
	v_rcp_f32_e32 v67, v67
	v_add_f32_e32 v65, 1.0, v85
	v_rcp_f32_e32 v66, v66
	v_mul_f32_e32 v82, v70, v83
	v_add_f32_e32 v64, 1.0, v84
	v_rcp_f32_e32 v65, v65
	v_mul_f32_e32 v91, v69, v82
	v_rcp_f32_e32 v64, v64
	v_mul_f32_e32 v90, v68, v91
	v_mul_f32_e32 v93, v67, v90
	v_mul_f32_e32 v92, v66, v93
	v_mul_f32_e32 v95, v65, v92
	v_mul_f32_e32 v94, v64, v95
	ds_bpermute_b32 v70, v132, v94
	ds_bpermute_b32 v71, v133, v94
	ds_bpermute_b32 v65, v134, v94
	ds_bpermute_b32 v64, v135, v94
	s_waitcnt lgkmcnt(0)
	v_mul_f32_e32 v157, v65, v64
	v_mul_f32_e32 v246, v157, v71
	v_cndmask_b32_e64 v158, 1.0, v64, s[10:11]
	v_cndmask_b32_e64 v158, v246, v158, s[14:15]
	v_cndmask_b32_e64 v158, v157, v158, s[12:13]
	v_med3_f32 v64, v76, s55, v123
	v_exp_f32_e32 v66, v64
	v_med3_f32 v64, v77, s55, v123
	v_exp_f32_e32 v67, v64
	v_med3_f32 v72, v72, s55, v123
	v_add_f32_e32 v64, 1.0, v66
	v_rcp_f32_e32 v68, v64
	v_med3_f32 v64, v78, s55, v123
	v_exp_f32_e32 v64, v64
	v_exp_f32_e32 v76, v72
	v_add_f32_e32 v65, 1.0, v67
	v_rcp_f32_e32 v69, v65
	v_add_f32_e32 v72, 1.0, v64
	v_rcp_f32_e32 v96, v72
	v_med3_f32 v72, v73, s55, v123
	v_exp_f32_e32 v77, v72
	v_med3_f32 v72, v74, s55, v123
	v_exp_f32_e32 v72, v72
	v_med3_f32 v73, v75, s55, v123
	v_exp_f32_e32 v73, v73
	v_med3_f32 v65, v79, s55, v123
	v_exp_f32_e32 v65, v65
	v_add_f32_e32 v75, 1.0, v72
	v_rcp_f32_e32 v97, v75
	v_add_f32_e32 v75, 1.0, v73
	v_add_f32_e32 v74, 1.0, v77
	v_rcp_f32_e32 v75, v75
	v_add_f32_e32 v79, 1.0, v76
	v_rcp_f32_e32 v154, v74
	v_add_f32_e32 v78, 1.0, v65
	v_rcp_f32_e32 v155, v79
	v_rcp_f32_e32 v156, v78
	v_mul_f32_e32 v74, v97, v75
	v_mul_f32_e32 v79, v154, v74
	v_mul_f32_e32 v78, v155, v79
	v_mul_f32_e32 v97, v156, v78
	v_mul_f32_e32 v96, v96, v97
	v_mul_f32_e32 v69, v69, v96
	v_mul_f32_e32 v68, v68, v69
	ds_bpermute_b32 v154, v132, v68
	ds_bpermute_b32 v155, v133, v68
	ds_bpermute_b32 v156, v134, v68
	ds_bpermute_b32 v160, v135, v68
	s_waitcnt lgkmcnt(0)
	v_mul_f32_e32 v156, v156, v160
	v_mul_f32_e32 v246, v156, v155
	v_cndmask_b32_e64 v159, 1.0, v160, s[10:11]
	v_cndmask_b32_e64 v159, v246, v159, s[14:15]
	v_cndmask_b32_e64 v159, v156, v159, s[12:13]
	s_and_b64 vcc, exec, s[8:9]
	s_cbranch_vccnz .LBB0_2052
	s_waitcnt vmcnt(3)
	ds_write_b128 v98, v[16:19] offset:16384
	s_waitcnt vmcnt(2)
	ds_write_b128 v99, v[20:23] offset:16384
	s_waitcnt vmcnt(1)
	ds_write_b128 v100, v[24:27] offset:32768
	s_waitcnt vmcnt(0)
	ds_write_b128 v124, v[28:31] offset:32768

.LBB0_2058:
	v_med3_f32 v73, v73, s55, v123
	v_exp_f32_e32 v73, v73
	v_med3_f32 v78, v78, s55, v123
	v_exp_f32_e32 v78, v78
	v_med3_f32 v79, v79, s55, v123
	v_med3_f32 v72, v72, s55, v123
	v_med3_f32 v77, v77, s55, v123
	v_exp_f32_e32 v79, v79
	v_exp_f32_e32 v72, v72
	v_med3_f32 v74, v74, s55, v123
	v_med3_f32 v76, v76, s55, v123
	v_exp_f32_e32 v77, v77
	v_add_f32_e32 v81, 1.0, v73
	v_exp_f32_e32 v74, v74
	v_med3_f32 v75, v75, s55, v123
	v_exp_f32_e32 v76, v76
	v_rcp_f32_e32 v87, v81
	v_exp_f32_e32 v75, v75
	v_add_f32_e32 v81, 1.0, v78
	v_rcp_f32_e32 v85, v81
	v_add_f32_e32 v81, 1.0, v79
	v_add_f32_e32 v80, 1.0, v72
	v_add_f32_e32 v83, 1.0, v77
	v_rcp_f32_e32 v81, v81
	v_rcp_f32_e32 v86, v80
	v_add_f32_e32 v80, 1.0, v74
	v_add_f32_e32 v82, 1.0, v76
	v_rcp_f32_e32 v83, v83
	v_rcp_f32_e32 v84, v80
	v_add_f32_e32 v80, 1.0, v75
	v_rcp_f32_e32 v82, v82
	v_rcp_f32_e32 v88, v80
	v_mul_f32_e32 v80, v85, v81
	v_mul_f32_e32 v83, v83, v80
	v_mul_f32_e32 v82, v82, v83
	v_mul_f32_e32 v85, v88, v82
	v_mul_f32_e32 v84, v84, v85
	v_mul_f32_e32 v87, v87, v84
	v_mul_f32_e32 v86, v86, v87
	ds_bpermute_b32 v96, v132, v86
	ds_bpermute_b32 v97, v133, v86
	ds_bpermute_b32 v89, v134, v86
	ds_bpermute_b32 v88, v135, v86
	s_waitcnt lgkmcnt(0)
	v_mul_f32_e32 v159, v89, v88
	v_mul_f32_e32 v246, v159, v97
	v_cndmask_b32_e64 v158, 1.0, v88, s[10:11]
	v_cndmask_b32_e64 v158, v246, v158, s[14:15]
	v_cndmask_b32_e64 v158, v159, v158, s[12:13]
	v_med3_f32 v69, v69, s55, v123
	v_exp_f32_e32 v69, v69
	v_med3_f32 v66, v66, s55, v123
	v_exp_f32_e32 v66, v66
	v_med3_f32 v67, v67, s55, v123
	v_med3_f32 v68, v68, s55, v123
	v_med3_f32 v65, v65, s55, v123
	v_exp_f32_e32 v67, v67
	v_exp_f32_e32 v68, v68
	v_med3_f32 v70, v70, s55, v123
	v_med3_f32 v64, v64, s55, v123
	v_exp_f32_e32 v65, v65
	v_add_f32_e32 v89, 1.0, v69
	v_exp_f32_e32 v70, v70
	v_med3_f32 v71, v71, s55, v123
	v_exp_f32_e32 v64, v64
	v_rcp_f32_e32 v95, v89
	v_exp_f32_e32 v71, v71
	v_add_f32_e32 v89, 1.0, v66
	v_rcp_f32_e32 v93, v89
	v_add_f32_e32 v89, 1.0, v67
	v_add_f32_e32 v88, 1.0, v68
	v_add_f32_e32 v91, 1.0, v65
	v_rcp_f32_e32 v89, v89
	v_rcp_f32_e32 v94, v88
	v_add_f32_e32 v88, 1.0, v70
	v_add_f32_e32 v90, 1.0, v64
	v_rcp_f32_e32 v91, v91
	v_rcp_f32_e32 v92, v88
	v_add_f32_e32 v88, 1.0, v71
	v_rcp_f32_e32 v90, v90
	v_rcp_f32_e32 v160, v88
	v_mul_f32_e32 v88, v93, v89
	v_mul_f32_e32 v91, v91, v88
	v_mul_f32_e32 v90, v90, v91
	v_mul_f32_e32 v93, v160, v90
	v_mul_f32_e32 v92, v92, v93
	v_mul_f32_e32 v95, v95, v92
	v_mul_f32_e32 v94, v94, v95
	ds_bpermute_b32 v160, v132, v94
	ds_bpermute_b32 v161, v133, v94
	ds_bpermute_b32 v162, v134, v94
	ds_bpermute_b32 v164, v135, v94
	s_waitcnt lgkmcnt(0)
	v_mul_f32_e32 v162, v162, v164
	v_mul_f32_e32 v246, v162, v161
	v_cndmask_b32_e64 v163, 1.0, v164, s[10:11]
	v_cndmask_b32_e64 v163, v246, v163, s[14:15]
	v_cndmask_b32_e64 v163, v162, v163, s[12:13]
	s_and_b64 vcc, exec, s[8:9]
	s_cbranch_vccnz .LBB0_2076
	s_waitcnt vmcnt(3)
	ds_write_b128 v98, v[16:19]
	s_waitcnt vmcnt(2)
	ds_write_b128 v99, v[20:23]
	s_waitcnt vmcnt(1)
	ds_write_b128 v100, v[24:27] offset:49152
	s_waitcnt vmcnt(0)
	ds_write_b128 v124, v[28:31] offset:49152

.LBB0_2161:
	v_med3_f32 v73, v73, s55, v123
	v_exp_f32_e32 v73, v73
	v_med3_f32 v78, v78, s55, v123
	v_exp_f32_e32 v78, v78
	v_med3_f32 v79, v79, s55, v123
	v_med3_f32 v72, v72, s55, v123
	v_med3_f32 v77, v77, s55, v123
	v_exp_f32_e32 v79, v79
	v_exp_f32_e32 v72, v72
	v_med3_f32 v74, v74, s55, v123
	v_med3_f32 v76, v76, s55, v123
	v_exp_f32_e32 v77, v77
	v_add_f32_e32 v81, 1.0, v73
	v_exp_f32_e32 v74, v74
	v_med3_f32 v75, v75, s55, v123
	v_exp_f32_e32 v76, v76
	v_rcp_f32_e32 v87, v81
	v_exp_f32_e32 v75, v75
	v_add_f32_e32 v81, 1.0, v78
	v_rcp_f32_e32 v85, v81
	v_add_f32_e32 v81, 1.0, v79
	v_add_f32_e32 v80, 1.0, v72
	v_add_f32_e32 v83, 1.0, v77
	v_rcp_f32_e32 v81, v81
	v_rcp_f32_e32 v86, v80
	v_add_f32_e32 v80, 1.0, v74
	v_add_f32_e32 v82, 1.0, v76
	v_rcp_f32_e32 v83, v83
	v_rcp_f32_e32 v84, v80
	v_add_f32_e32 v80, 1.0, v75
	v_rcp_f32_e32 v82, v82
	v_rcp_f32_e32 v88, v80
	v_mul_f32_e32 v80, v85, v81
	v_mul_f32_e32 v83, v83, v80
	v_mul_f32_e32 v82, v82, v83
	v_mul_f32_e32 v85, v88, v82
	v_mul_f32_e32 v84, v84, v85
	v_mul_f32_e32 v87, v87, v84
	v_mul_f32_e32 v86, v86, v87
	ds_bpermute_b32 v96, v132, v86
	ds_bpermute_b32 v97, v133, v86
	ds_bpermute_b32 v89, v134, v86
	ds_bpermute_b32 v88, v135, v86
	s_waitcnt lgkmcnt(0)
	v_mul_f32_e32 v159, v89, v88
	v_mul_f32_e32 v246, v159, v97
	v_cndmask_b32_e64 v158, 1.0, v88, s[10:11]
	v_cndmask_b32_e64 v158, v246, v158, s[14:15]
	v_cndmask_b32_e64 v158, v159, v158, s[12:13]
	v_med3_f32 v69, v69, s55, v123
	v_exp_f32_e32 v69, v69
	v_med3_f32 v68, v68, s55, v123
	v_exp_f32_e32 v68, v68
	v_med3_f32 v65, v65, s55, v123
	v_add_f32_e32 v89, 1.0, v69
	v_rcp_f32_e32 v161, v89
	v_exp_f32_e32 v89, v65
	v_med3_f32 v65, v66, s55, v123
	v_exp_f32_e32 v90, v65
	v_med3_f32 v65, v67, s55, v123
	v_exp_f32_e32 v91, v65
	v_add_f32_e32 v88, 1.0, v68
	v_med3_f32 v64, v64, s55, v123
	v_rcp_f32_e32 v160, v88
	v_med3_f32 v71, v71, s55, v123
	v_exp_f32_e32 v88, v64
	v_med3_f32 v70, v70, s55, v123
	v_exp_f32_e32 v71, v71
	v_exp_f32_e32 v70, v70
	v_add_f32_e32 v66, 1.0, v90
	v_add_f32_e32 v67, 1.0, v91
	v_add_f32_e32 v65, 1.0, v89
	v_rcp_f32_e32 v66, v66
	v_rcp_f32_e32 v93, v67
	v_add_f32_e32 v94, 1.0, v88
	v_rcp_f32_e32 v65, v65
	v_add_f32_e32 v92, 1.0, v71
	v_rcp_f32_e32 v94, v94
	v_add_f32_e32 v64, 1.0, v70
	v_rcp_f32_e32 v95, v92
	v_rcp_f32_e32 v64, v64
	v_mul_f32_e32 v92, v66, v93
	v_mul_f32_e32 v67, v65, v92
	v_mul_f32_e32 v66, v94, v67
	v_mul_f32_e32 v95, v95, v66
	v_mul_f32_e32 v94, v64, v95
	v_mul_f32_e32 v65, v161, v94
	v_mul_f32_e32 v64, v160, v65
	ds_bpermute_b32 v160, v132, v64
	ds_bpermute_b32 v161, v133, v64
	ds_bpermute_b32 v162, v134, v64
	ds_bpermute_b32 v164, v135, v64
	s_waitcnt lgkmcnt(0)
	v_mul_f32_e32 v162, v162, v164
	v_mul_f32_e32 v246, v162, v161
	v_cndmask_b32_e64 v163, 1.0, v164, s[10:11]
	v_cndmask_b32_e64 v163, v246, v163, s[14:15]
	v_cndmask_b32_e64 v163, v162, v163, s[12:13]
	s_and_b64 vcc, exec, s[8:9]
	s_cbranch_vccnz .LBB0_2179
	s_waitcnt vmcnt(3)
	ds_write_b128 v98, v[16:19]
	s_waitcnt vmcnt(2)
	ds_write_b128 v99, v[20:23]
	s_waitcnt vmcnt(1)
	ds_write_b128 v100, v[24:27] offset:49152
	s_waitcnt vmcnt(0)
	ds_write_b128 v124, v[28:31] offset:49152

.LBB0_2285:
	v_mov_b64_e32 v[146:147], s[16:17]
	v_mad_i64_i32 v[244:245], s[28:29], v128, s48, v[146:147]
	v_lshl_or_b32 v138, s0, 8, v153
	v_ashrrev_i32_e32 v139, 31, v138
	v_lshlrev_b64 v[242:243], 1, v[138:139]
	v_lshl_add_u64 v[240:241], v[244:245], 0, v[242:243]
	global_load_dwordx4 v[140:143], v[240:241], off
	global_load_dwordx4 v[160:163], v[240:241], off offset:256
	v_or_b32_e32 v244, 16, v128
	v_mad_i64_i32 v[138:139], s[28:29], v244, s48, v[146:147]
	v_lshl_add_u64 v[240:241], v[138:139], 0, v[242:243]
	global_load_dwordx4 v[164:167], v[240:241], off
	global_load_dwordx4 v[168:171], v[240:241], off offset:256
	v_or_b32_e32 v138, 32, v128
	v_mad_i64_i32 v[238:239], s[28:29], v138, s48, v[146:147]
	v_lshl_add_u64 v[240:241], v[238:239], 0, v[242:243]
	global_load_dwordx4 v[172:175], v[240:241], off
	global_load_dwordx4 v[176:179], v[240:241], off offset:256
	v_or_b32_e32 v238, 48, v128
	v_mad_i64_i32 v[236:237], s[28:29], v238, s48, v[146:147]
	v_lshl_add_u64 v[240:241], v[236:237], 0, v[242:243]
	global_load_dwordx4 v[180:183], v[240:241], off
	global_load_dwordx4 v[184:187], v[240:241], off offset:256
	v_add_u32_e32 v236, 0x80, v128
	v_mad_i64_i32 v[234:235], s[28:29], v236, s48, v[146:147]
	v_lshl_add_u64 v[240:241], v[234:235], 0, v[242:243]
	global_load_dwordx4 v[188:191], v[240:241], off
	global_load_dwordx4 v[192:195], v[240:241], off offset:256
	v_add_u32_e32 v234, 0x90, v128
	v_mad_i64_i32 v[232:233], s[28:29], v234, s48, v[146:147]
	v_lshl_add_u64 v[240:241], v[232:233], 0, v[242:243]
	global_load_dwordx4 v[196:199], v[240:241], off
	global_load_dwordx4 v[200:203], v[240:241], off offset:256
	v_ashrrev_i32_e32 v129, 31, v128
	v_lshlrev_b64 v[232:233], 12, v[128:129]
	v_lshl_add_u64 v[240:241], s[8:9], 0, v[232:233]
	v_lshl_add_u64 v[230:231], v[240:241], 0, v[242:243]
	s_waitcnt vmcnt(11)
	v_lshlrev_b32_e32 v228, 16, v140
	v_and_b32_e32 v229, 0xffff0000, v140
	v_lshlrev_b32_e32 v240, 16, v141
	v_and_b32_e32 v241, 0xffff0000, v141
	v_lshlrev_b32_e32 v232, 16, v142
	v_and_b32_e32 v233, 0xffff0000, v142
	v_lshlrev_b32_e32 v226, 16, v143
	v_and_b32_e32 v227, 0xffff0000, v143
	v_pk_mul_f32 v[224:225], v[108:109], v[228:229]
	v_pk_mul_f32 v[222:223], v[110:111], v[240:241]
	v_pk_mul_f32 v[220:221], v[104:105], v[232:233]
	v_pk_mul_f32 v[228:229], v[106:107], v[226:227]
	v_cvt_pk_bf16_f32 v140, v224, v225
	v_cvt_pk_bf16_f32 v141, v222, v223
	v_cvt_pk_bf16_f32 v142, v220, v221
	v_cvt_pk_bf16_f32 v143, v228, v229
	global_store_dwordx4 v[230:231], v[140:143], off
	v_add_u32_e32 v240, 0xa0, v128
	v_mad_i64_i32 v[232:233], s[28:29], v240, s48, v[146:147]
	v_lshl_add_u64 v[228:229], v[232:233], 0, v[242:243]
	global_load_dwordx4 v[140:143], v[228:229], off
	v_ashrrev_i32_e32 v245, 31, v244
	v_lshlrev_b64 v[232:233], 12, v[244:245]
	v_lshl_add_u64 v[226:227], s[8:9], 0, v[232:233]
	v_lshl_add_u64 v[224:225], v[226:227], 0, v[242:243]
	s_waitcnt vmcnt(12)
	v_lshlrev_b32_e32 v244, 16, v160
	v_and_b32_e32 v245, 0xffff0000, v160
	v_lshlrev_b32_e32 v232, 16, v161
	v_and_b32_e32 v233, 0xffff0000, v161
	v_lshlrev_b32_e32 v226, 16, v162
	v_and_b32_e32 v227, 0xffff0000, v162
	v_lshlrev_b32_e32 v222, 16, v163
	v_and_b32_e32 v223, 0xffff0000, v163
	v_pk_mul_f32 v[220:221], v[76:77], v[244:245]
	v_pk_mul_f32 v[218:219], v[78:79], v[232:233]
	v_pk_mul_f32 v[216:217], v[72:73], v[226:227]
	v_pk_mul_f32 v[244:245], v[74:75], v[222:223]
	v_cvt_pk_bf16_f32 v160, v220, v221
	v_cvt_pk_bf16_f32 v161, v218, v219
	v_cvt_pk_bf16_f32 v162, v216, v217
	v_cvt_pk_bf16_f32 v163, v244, v245
	global_store_dwordx4 v[230:231], v[160:163], off offset:256
	global_load_dwordx4 v[204:207], v[228:229], off offset:256
	s_waitcnt vmcnt(13)
	v_lshlrev_b32_e32 v232, 16, v164
	v_and_b32_e32 v233, 0xffff0000, v164
	v_lshlrev_b32_e32 v226, 16, v165
	v_and_b32_e32 v227, 0xffff0000, v165
	v_lshlrev_b32_e32 v244, 16, v166
	v_and_b32_e32 v245, 0xffff0000, v166
	v_lshlrev_b32_e32 v230, 16, v167
	v_and_b32_e32 v231, 0xffff0000, v167
	v_pk_mul_f32 v[228:229], v[100:101], v[232:233]
	v_pk_mul_f32 v[222:223], v[102:103], v[226:227]
	v_pk_mul_f32 v[220:221], v[96:97], v[244:245]
	v_pk_mul_f32 v[232:233], v[98:99], v[230:231]
	v_cvt_pk_bf16_f32 v160, v228, v229
	v_cvt_pk_bf16_f32 v161, v222, v223
	v_cvt_pk_bf16_f32 v162, v220, v221
	v_cvt_pk_bf16_f32 v163, v232, v233
	global_store_dwordx4 v[224:225], v[160:163], off
	v_add_u32_e32 v226, 0xb0, v128
	v_mad_i64_i32 v[232:233], s[28:29], v226, s48, v[146:147]
	v_lshl_add_u64 v[244:245], v[232:233], 0, v[242:243]
	global_load_dwordx4 v[162:165], v[244:245], off
	v_ashrrev_i32_e32 v139, 31, v138
	s_waitcnt vmcnt(14)
	v_lshlrev_b32_e32 v232, 16, v168
	v_and_b32_e32 v233, 0xffff0000, v168
	v_lshlrev_b32_e32 v166, 16, v169
	v_and_b32_e32 v167, 0xffff0000, v169
	v_lshlrev_b32_e32 v160, 16, v170
	v_and_b32_e32 v161, 0xffff0000, v170
	v_lshlrev_b32_e32 v146, 16, v171
	v_and_b32_e32 v147, 0xffff0000, v171
	v_pk_mul_f32 v[230:231], v[68:69], v[232:233]
	v_pk_mul_f32 v[228:229], v[70:71], v[166:167]
	v_pk_mul_f32 v[222:223], v[64:65], v[160:161]
	v_pk_mul_f32 v[232:233], v[66:67], v[146:147]
	v_cvt_pk_bf16_f32 v168, v230, v231
	v_cvt_pk_bf16_f32 v169, v228, v229
	v_cvt_pk_bf16_f32 v170, v222, v223
	v_cvt_pk_bf16_f32 v171, v232, v233
	global_store_dwordx4 v[224:225], v[168:171], off offset:256
	global_load_dwordx4 v[210:213], v[244:245], off offset:256
	v_lshlrev_b64 v[232:233], 12, v[138:139]
	v_lshl_add_u64 v[224:225], s[8:9], 0, v[232:233]
	v_lshl_add_u64 v[214:215], v[224:225], 0, v[242:243]
	s_waitcnt vmcnt(15)
	v_lshlrev_b32_e32 v208, 16, v172
	v_and_b32_e32 v209, 0xffff0000, v172
	v_lshlrev_b32_e32 v232, 16, v173
	v_and_b32_e32 v233, 0xffff0000, v173
	v_lshlrev_b32_e32 v224, 16, v174
	v_and_b32_e32 v225, 0xffff0000, v174
	v_lshlrev_b32_e32 v166, 16, v175
	v_and_b32_e32 v167, 0xffff0000, v175
	v_pk_mul_f32 v[160:161], v[92:93], v[208:209]
	v_pk_mul_f32 v[146:147], v[94:95], v[232:233]
	v_pk_mul_f32 v[244:245], v[88:89], v[224:225]
	v_pk_mul_f32 v[208:209], v[90:91], v[166:167]
	v_cvt_pk_bf16_f32 v168, v160, v161
	v_cvt_pk_bf16_f32 v169, v146, v147
	v_cvt_pk_bf16_f32 v170, v244, v245
	v_cvt_pk_bf16_f32 v171, v208, v209
	global_store_dwordx4 v[214:215], v[168:171], off
	v_ashrrev_i32_e32 v239, 31, v238
	s_waitcnt vmcnt(15)
	v_lshlrev_b32_e32 v232, 16, v176
	v_and_b32_e32 v233, 0xffff0000, v176
	v_lshlrev_b32_e32 v224, 16, v177
	v_and_b32_e32 v225, 0xffff0000, v177
	v_lshlrev_b32_e32 v208, 16, v178
	v_and_b32_e32 v209, 0xffff0000, v178
	v_lshlrev_b32_e32 v166, 16, v179
	v_and_b32_e32 v167, 0xffff0000, v179
	v_pk_mul_f32 v[160:161], v[60:61], v[232:233]
	v_pk_mul_f32 v[146:147], v[62:63], v[224:225]
	v_pk_mul_f32 v[244:245], v[56:57], v[208:209]
	v_pk_mul_f32 v[232:233], v[58:59], v[166:167]
	v_cvt_pk_bf16_f32 v168, v160, v161
	v_cvt_pk_bf16_f32 v169, v146, v147
	v_cvt_pk_bf16_f32 v170, v244, v245
	v_cvt_pk_bf16_f32 v171, v232, v233
	global_store_dwordx4 v[214:215], v[168:171], off offset:256
	v_lshlrev_b64 v[224:225], 12, v[238:239]
	v_lshl_add_u64 v[232:233], s[8:9], 0, v[224:225]
	v_lshl_add_u64 v[214:215], v[232:233], 0, v[242:243]
	s_waitcnt vmcnt(15)
	v_lshlrev_b32_e32 v238, 16, v180
	v_and_b32_e32 v239, 0xffff0000, v180
	v_lshlrev_b32_e32 v232, 16, v181
	v_and_b32_e32 v233, 0xffff0000, v181
	v_lshlrev_b32_e32 v224, 16, v182
	v_and_b32_e32 v225, 0xffff0000, v182
	v_lshlrev_b32_e32 v208, 16, v183
	v_and_b32_e32 v209, 0xffff0000, v183
	v_pk_mul_f32 v[166:167], v[84:85], v[238:239]
	v_pk_mul_f32 v[160:161], v[86:87], v[232:233]
	v_pk_mul_f32 v[146:147], v[80:81], v[224:225]
	v_pk_mul_f32 v[238:239], v[82:83], v[208:209]
	v_cvt_pk_bf16_f32 v168, v166, v167
	v_cvt_pk_bf16_f32 v169, v160, v161
	v_cvt_pk_bf16_f32 v170, v146, v147
	v_cvt_pk_bf16_f32 v171, v238, v239
	global_store_dwordx4 v[214:215], v[168:171], off
	v_ashrrev_i32_e32 v237, 31, v236
	s_waitcnt vmcnt(15)
	v_lshlrev_b32_e32 v238, 16, v184
	v_and_b32_e32 v239, 0xffff0000, v184
	v_lshlrev_b32_e32 v232, 16, v185
	v_and_b32_e32 v233, 0xffff0000, v185
	v_lshlrev_b32_e32 v224, 16, v186
	v_and_b32_e32 v225, 0xffff0000, v186
	v_lshlrev_b32_e32 v208, 16, v187
	v_and_b32_e32 v209, 0xffff0000, v187
	v_pk_mul_f32 v[166:167], v[52:53], v[238:239]
	v_pk_mul_f32 v[160:161], v[54:55], v[232:233]
	v_pk_mul_f32 v[146:147], v[48:49], v[224:225]
	v_pk_mul_f32 v[238:239], v[50:51], v[208:209]
	v_cvt_pk_bf16_f32 v168, v166, v167
	v_cvt_pk_bf16_f32 v169, v160, v161
	v_cvt_pk_bf16_f32 v170, v146, v147
	v_cvt_pk_bf16_f32 v171, v238, v239
	global_store_dwordx4 v[214:215], v[168:171], off offset:256
	v_lshlrev_b64 v[232:233], 12, v[236:237]
	v_lshl_add_u64 v[224:225], s[8:9], 0, v[232:233]
	v_lshl_add_u64 v[214:215], v[224:225], 0, v[242:243]
	s_waitcnt vmcnt(15)
	v_lshlrev_b32_e32 v208, 16, v188
	v_and_b32_e32 v209, 0xffff0000, v188
	v_lshlrev_b32_e32 v232, 16, v189
	v_and_b32_e32 v233, 0xffff0000, v189
	v_lshlrev_b32_e32 v224, 16, v190
	v_and_b32_e32 v225, 0xffff0000, v190
	v_lshlrev_b32_e32 v166, 16, v191
	v_and_b32_e32 v167, 0xffff0000, v191
	v_pk_mul_f32 v[160:161], v[44:45], v[208:209]
	v_pk_mul_f32 v[146:147], v[46:47], v[232:233]
	v_pk_mul_f32 v[244:245], v[40:41], v[224:225]
	v_pk_mul_f32 v[208:209], v[42:43], v[166:167]
	v_cvt_pk_bf16_f32 v168, v160, v161
	v_cvt_pk_bf16_f32 v169, v146, v147
	v_cvt_pk_bf16_f32 v170, v244, v245
	v_cvt_pk_bf16_f32 v171, v208, v209
	global_store_dwordx4 v[214:215], v[168:171], off
	v_ashrrev_i32_e32 v235, 31, v234
	s_waitcnt vmcnt(15)
	v_lshlrev_b32_e32 v232, 16, v192
	v_and_b32_e32 v233, 0xffff0000, v192
	v_lshlrev_b32_e32 v224, 16, v193
	v_and_b32_e32 v225, 0xffff0000, v193
	v_lshlrev_b32_e32 v208, 16, v194
	v_and_b32_e32 v209, 0xffff0000, v194
	v_lshlrev_b32_e32 v166, 16, v195
	v_and_b32_e32 v167, 0xffff0000, v195
	v_pk_mul_f32 v[160:161], v[12:13], v[232:233]
	v_pk_mul_f32 v[146:147], v[14:15], v[224:225]
	v_pk_mul_f32 v[244:245], v[8:9], v[208:209]
	v_pk_mul_f32 v[232:233], v[10:11], v[166:167]
	v_cvt_pk_bf16_f32 v168, v160, v161
	v_cvt_pk_bf16_f32 v169, v146, v147
	v_cvt_pk_bf16_f32 v170, v244, v245
	v_cvt_pk_bf16_f32 v171, v232, v233
	global_store_dwordx4 v[214:215], v[168:171], off offset:256
	v_lshlrev_b64 v[224:225], 12, v[234:235]
	v_lshl_add_u64 v[208:209], s[8:9], 0, v[224:225]
	v_lshl_add_u64 v[214:215], v[208:209], 0, v[242:243]
	s_waitcnt vmcnt(15)
	v_lshlrev_b32_e32 v166, 16, v196
	v_and_b32_e32 v167, 0xffff0000, v196
	v_lshlrev_b32_e32 v224, 16, v197
	v_and_b32_e32 v225, 0xffff0000, v197
	v_lshlrev_b32_e32 v208, 16, v198
	v_and_b32_e32 v209, 0xffff0000, v198
	v_lshlrev_b32_e32 v160, 16, v199
	v_and_b32_e32 v161, 0xffff0000, v199
	v_pk_mul_f32 v[146:147], v[36:37], v[166:167]
	v_pk_mul_f32 v[244:245], v[38:39], v[224:225]
	v_pk_mul_f32 v[138:139], v[32:33], v[208:209]
	v_pk_mul_f32 v[166:167], v[34:35], v[160:161]
	v_cvt_pk_bf16_f32 v168, v146, v147
	v_cvt_pk_bf16_f32 v169, v244, v245
	v_cvt_pk_bf16_f32 v170, v138, v139
	v_cvt_pk_bf16_f32 v171, v166, v167
	global_store_dwordx4 v[214:215], v[168:171], off
	v_ashrrev_i32_e32 v241, 31, v240
	s_waitcnt vmcnt(15)
	v_lshlrev_b32_e32 v224, 16, v200
	v_and_b32_e32 v225, 0xffff0000, v200
	v_lshlrev_b32_e32 v208, 16, v201
	v_and_b32_e32 v209, 0xffff0000, v201
	v_lshlrev_b32_e32 v166, 16, v202
	v_and_b32_e32 v167, 0xffff0000, v202
	v_lshlrev_b32_e32 v160, 16, v203
	v_and_b32_e32 v161, 0xffff0000, v203
	v_pk_mul_f32 v[146:147], v[4:5], v[224:225]
	v_pk_mul_f32 v[244:245], v[6:7], v[208:209]
	v_pk_mul_f32 v[138:139], v[0:1], v[166:167]
	v_pk_mul_f32 v[224:225], v[2:3], v[160:161]
	v_cvt_pk_bf16_f32 v168, v146, v147
	v_cvt_pk_bf16_f32 v169, v244, v245
	v_cvt_pk_bf16_f32 v170, v138, v139
	v_cvt_pk_bf16_f32 v171, v224, v225
	global_store_dwordx4 v[214:215], v[168:171], off offset:256
	v_lshlrev_b64 v[208:209], 12, v[240:241]
	v_lshl_add_u64 v[224:225], s[8:9], 0, v[208:209]
	v_lshl_add_u64 v[214:215], v[224:225], 0, v[242:243]
	s_waitcnt vmcnt(14)
	v_lshlrev_b32_e32 v240, 16, v140
	v_and_b32_e32 v241, 0xffff0000, v140
	v_lshlrev_b32_e32 v224, 16, v141
	v_and_b32_e32 v225, 0xffff0000, v141
	v_lshlrev_b32_e32 v208, 16, v142
	v_and_b32_e32 v209, 0xffff0000, v142
	v_lshlrev_b32_e32 v166, 16, v143
	v_and_b32_e32 v167, 0xffff0000, v143
	v_pk_mul_f32 v[160:161], v[28:29], v[240:241]
	v_pk_mul_f32 v[146:147], v[30:31], v[224:225]
	v_pk_mul_f32 v[244:245], v[24:25], v[208:209]
	v_pk_mul_f32 v[240:241], v[26:27], v[166:167]
	v_cvt_pk_bf16_f32 v140, v160, v161
	v_cvt_pk_bf16_f32 v141, v146, v147
	v_cvt_pk_bf16_f32 v142, v244, v245
	v_cvt_pk_bf16_f32 v143, v240, v241
	global_store_dwordx4 v[214:215], v[140:143], off
	v_ashrrev_i32_e32 v227, 31, v226
	s_waitcnt vmcnt(13)
	v_lshlrev_b32_e32 v240, 16, v204
	v_and_b32_e32 v241, 0xffff0000, v204
	v_lshlrev_b32_e32 v224, 16, v205
	v_and_b32_e32 v225, 0xffff0000, v205
	v_lshlrev_b32_e32 v208, 16, v206
	v_and_b32_e32 v209, 0xffff0000, v206
	v_lshlrev_b32_e32 v166, 16, v207
	v_and_b32_e32 v167, 0xffff0000, v207
	v_pk_mul_f32 v[160:161], v[112:113], v[240:241]
	v_pk_mul_f32 v[146:147], v[114:115], v[224:225]
	v_pk_mul_f32 v[244:245], v[116:117], v[208:209]
	v_pk_mul_f32 v[240:241], v[118:119], v[166:167]
	v_cvt_pk_bf16_f32 v138, v160, v161
	v_cvt_pk_bf16_f32 v139, v146, v147
	v_cvt_pk_bf16_f32 v140, v244, v245
	v_cvt_pk_bf16_f32 v141, v240, v241
	global_store_dwordx4 v[214:215], v[138:141], off offset:256
	v_lshlrev_b64 v[224:225], 12, v[226:227]
	v_lshl_add_u64 v[240:241], s[8:9], 0, v[224:225]
	v_lshl_add_u64 v[130:131], v[240:241], 0, v[242:243]
	s_waitcnt vmcnt(12)
	v_lshlrev_b32_e32 v214, 16, v162
	v_and_b32_e32 v215, 0xffff0000, v162
	v_lshlrev_b32_e32 v208, 16, v163
	v_and_b32_e32 v209, 0xffff0000, v163
	v_lshlrev_b32_e32 v166, 16, v164
	v_and_b32_e32 v167, 0xffff0000, v164
	v_lshlrev_b32_e32 v160, 16, v165
	v_and_b32_e32 v161, 0xffff0000, v165
	v_pk_mul_f32 v[146:147], v[20:21], v[214:215]
	v_pk_mul_f32 v[244:245], v[22:23], v[208:209]
	v_pk_mul_f32 v[164:165], v[16:17], v[166:167]
	v_pk_mul_f32 v[214:215], v[18:19], v[160:161]
	v_cvt_pk_bf16_f32 v138, v146, v147
	v_cvt_pk_bf16_f32 v139, v244, v245
	v_cvt_pk_bf16_f32 v140, v164, v165
	v_cvt_pk_bf16_f32 v141, v214, v215
	global_store_dwordx4 v[130:131], v[138:141], off
	s_waitcnt vmcnt(11)
	v_lshlrev_b32_e32 v208, 16, v210
	v_and_b32_e32 v209, 0xffff0000, v210
	v_lshlrev_b32_e32 v214, 16, v211
	v_and_b32_e32 v215, 0xffff0000, v211
	v_lshlrev_b32_e32 v146, 16, v212
	v_and_b32_e32 v147, 0xffff0000, v212
	v_lshlrev_b32_e32 v244, 16, v213
	v_and_b32_e32 v245, 0xffff0000, v213
	v_pk_mul_f32 v[138:139], v[120:121], v[208:209]
	v_pk_mul_f32 v[242:243], v[122:123], v[214:215]
	v_pk_mul_f32 v[240:241], v[124:125], v[146:147]
	v_pk_mul_f32 v[238:239], v[126:127], v[244:245]
	v_cvt_pk_bf16_f32 v162, v138, v139
	v_cvt_pk_bf16_f32 v163, v242, v243
	v_cvt_pk_bf16_f32 v164, v240, v241
	v_cvt_pk_bf16_f32 v165, v238, v239
	global_store_dwordx4 v[130:131], v[162:165], off offset:256
	s_cbranch_execnz .LBB0_2284
